# stack: counters + rope preload IN0/IN1 + LN gain/bias preload in combine phases + unrolled prologue conversion + ATT1 batched LDS fragment reads
# speedup vs baseline: 1.0022x; 1.0022x over previous
.LBB0_7:
	s_or_b64 exec, exec, s[2:3]
	s_getreg_b32 s2, hwreg(HW_REG_HW_ID, 0, 6)
	s_lshl_b32 s2, s2, 2
	s_add_i32 s2, s2, 0x27000
	v_mov_b32_e32 v1, s2
	ds_read_b32 v1, v1
	s_mov_b32 s73, 0
	v_mbcnt_lo_u32_b32 v0, -1, v0
	v_mbcnt_hi_u32_b32 v0, -1, v0
	s_waitcnt lgkmcnt(0)
	v_readfirstlane_b32 s4, v1
	s_lshl_b64 s[2:3], s[72:73], 9
	s_load_dwordx16 s[16:31], s[0:1], 0x0
	v_lshl_or_b32 v2, s4, 6, v0
	s_load_dword s4, s[0:1], 0xd8
	v_ashrrev_i32_e32 v3, 31, v2
	v_lshl_add_u64 v[0:1], s[2:3], 0, v[2:3]
	s_add_u32 s2, s0, 0xd8
	s_addc_u32 s3, s1, 0
	s_mov_b32 s5, s73
	v_writelane_b32 v253, s2, 0
	s_nop 1
	v_writelane_b32 v253, s3, 1
	s_waitcnt lgkmcnt(0)
	v_writelane_b32 v253, s4, 2
	s_mov_b64 s[2:3], 0x200000
	s_lshl_b64 s[10:11], s[4:5], 9
	v_writelane_b32 v253, s5, 3
	v_cmp_gt_u64_e32 vcc, s[2:3], v[0:1]
	s_and_saveexec_b64 s[2:3], vcc
	s_cbranch_execz .LBB0_10
	s_lshl_b64 s[4:5], s[72:73], 13
	s_add_u32 s4, s70, s4
	s_addc_u32 s5, s71, s5
	v_readlane_b32 s8, v253, 2
	v_lshl_add_u64 v[4:5], v[2:3], 4, s[4:5]
	s_mov_b64 s[4:5], 0x10d500
	v_readlane_b32 s9, v253, 3
	v_lshl_add_u64 v[4:5], v[4:5], 0, s[4:5]
	s_lshl_b64 s[4:5], s[8:9], 13
	s_lshl_b64 s[6:7], s[72:73], 14
	s_add_u32 s6, s16, s6
	v_lshlrev_b64 v[6:7], 5, v[2:3]
	s_addc_u32 s7, s17, s7
	v_lshl_add_u64 v[6:7], s[6:7], 0, v[6:7]
	v_lshl_add_u64 v[6:7], v[6:7], 0, 16
	s_lshl_b64 s[6:7], s[8:9], 14
	s_mov_b64 s[8:9], 0
	s_mov_b64 s[12:13], 0x1fffff
	v_mov_b64_e32 v[8:9], v[0:1]
	s_cmp_eq_u32 s10, 0x20000
	s_cbranch_scc0 .LBB0_9
	s_cmp_eq_u32 s11, 0
	s_cbranch_scc0 .LBB0_9
	s_mov_b32 s98, 4
.Lopt10_x4:
	global_load_dwordx4 v[10:13], v[6:7], off offset:-16
	global_load_dwordx4 v[14:17], v[6:7], off
	v_lshl_add_u64 v[6:7], v[6:7], 0, s[6:7]
	global_load_dwordx4 v[18:21], v[6:7], off offset:-16
	global_load_dwordx4 v[22:25], v[6:7], off
	v_lshl_add_u64 v[6:7], v[6:7], 0, s[6:7]
	global_load_dwordx4 v[26:29], v[6:7], off offset:-16
	global_load_dwordx4 v[30:33], v[6:7], off
	v_lshl_add_u64 v[6:7], v[6:7], 0, s[6:7]
	global_load_dwordx4 v[34:37], v[6:7], off offset:-16
	global_load_dwordx4 v[38:41], v[6:7], off
	v_lshl_add_u64 v[6:7], v[6:7], 0, s[6:7]
	s_waitcnt vmcnt(6)
	v_cvt_pk_bf16_f32 v10, v10, v11
	v_cvt_pk_bf16_f32 v11, v12, v13
	v_cvt_pk_bf16_f32 v12, v14, v15
	v_cvt_pk_bf16_f32 v13, v16, v17
	global_store_dwordx4 v[4:5], v[10:13], off
	v_lshl_add_u64 v[4:5], v[4:5], 0, s[4:5]
	s_waitcnt vmcnt(5)
	v_cvt_pk_bf16_f32 v18, v18, v19
	v_cvt_pk_bf16_f32 v19, v20, v21
	v_cvt_pk_bf16_f32 v20, v22, v23
	v_cvt_pk_bf16_f32 v21, v24, v25
	global_store_dwordx4 v[4:5], v[18:21], off
	v_lshl_add_u64 v[4:5], v[4:5], 0, s[4:5]
	s_waitcnt vmcnt(4)
	v_cvt_pk_bf16_f32 v26, v26, v27
	v_cvt_pk_bf16_f32 v27, v28, v29
	v_cvt_pk_bf16_f32 v28, v30, v31
	v_cvt_pk_bf16_f32 v29, v32, v33
	global_store_dwordx4 v[4:5], v[26:29], off
	v_lshl_add_u64 v[4:5], v[4:5], 0, s[4:5]
	s_waitcnt vmcnt(3)
	v_cvt_pk_bf16_f32 v34, v34, v35
	v_cvt_pk_bf16_f32 v35, v36, v37
	v_cvt_pk_bf16_f32 v36, v38, v39
	v_cvt_pk_bf16_f32 v37, v40, v41
	global_store_dwordx4 v[4:5], v[34:37], off
	v_lshl_add_u64 v[4:5], v[4:5], 0, s[4:5]
	s_sub_u32 s98, s98, 1
	s_cmp_lg_u32 s98, 0
	s_cbranch_scc1 .Lopt10_x4
	s_branch .LBB0_10

.LBB0_1009:
	s_or_b64 exec, exec, s[0:1]
	v_ashrrev_i32_e32 v0, 6, v3
	v_readlane_b32 s0, v253, 30
	s_waitcnt lgkmcnt(0)
	s_barrier
	v_add_u32_e32 v80, s0, v0
	s_movk_i32 s0, 0x4000
	v_cmp_gt_i32_e32 vcc, s0, v80
	s_and_saveexec_b64 s[2:3], vcc
	s_cbranch_execz .LBB0_1014
	v_readlane_b32 s4, v253, 4
	v_and_b32_e32 v1, 63, v2
	v_readlane_b32 s5, v253, 5
	v_lshlrev_b32_e32 v2, 5, v1
	v_mov_b32_e32 v3, 0
	v_readlane_b32 s18, v253, 18
	v_readlane_b32 s19, v253, 19
	v_readlane_b32 s4, v254, 3
	v_lshl_add_u64 v[84:85], s[64:65], 0, v[2:3]
	v_lshl_add_u64 v[82:83], s[18:19], 0, v[2:3]
	v_lshlrev_b32_e32 v2, 4, v1
	v_readlane_b32 s5, v254, 4
	v_lshlrev_b32_e32 v0, 3, v0
	v_ashrrev_i32_e32 v81, 31, v80
	v_lshl_add_u64 v[86:87], s[4:5], 0, v[2:3]
	s_lshl_b32 s4, s72, 6
	v_cmp_gt_u32_e64 s[0:1], 8, v1
	v_add3_u32 v88, s4, v0, v1
	v_readlane_b32 s4, v253, 2
	v_lshlrev_b64 v[0:1], 11, v[80:81]
	v_readlane_b32 s9, v253, 9
	v_readlane_b32 s5, v253, 3
	v_or_b32_e32 v0, v0, v2
	v_readlane_b32 s6, v253, 6
	v_readlane_b32 s7, v253, 7
	v_readlane_b32 s8, v253, 8
	s_lshl_b32 s9, s4, 6
	v_lshl_add_u64 v[0:1], s[70:71], 0, v[0:1]
	s_mov_b64 s[4:5], 0xd60d500
	s_ashr_i32 s75, s74, 31
	v_lshl_add_u64 v[90:91], v[0:1], 0, s[4:5]
	s_lshl_b64 s[4:5], s[74:75], 11
	s_mov_b64 s[6:7], 0
	s_mov_b32 s8, 0x3fb504f3
	v_mov_b32_e32 v81, 0x3727c5ac
	v_readlane_b32 s10, v253, 10
	v_readlane_b32 s11, v253, 11
	v_readlane_b32 s12, v253, 12
	v_readlane_b32 s13, v253, 13
	v_readlane_b32 s14, v253, 14
	v_readlane_b32 s15, v253, 15
	v_readlane_b32 s16, v253, 16
	v_readlane_b32 s17, v253, 17
	global_load_dwordx4 v[200:203], v[82:83], off
	global_load_dwordx4 v[204:207], v[82:83], off offset:16
	global_load_dwordx4 v[208:211], v[84:85], off
	global_load_dwordx4 v[212:215], v[84:85], off offset:16
	global_load_dwordx4 v[216:219], v[82:83], off offset:2048
	global_load_dwordx4 v[220:223], v[82:83], off offset:2064
	global_load_dwordx4 v[224:227], v[84:85], off offset:2048
	global_load_dwordx4 v[228:231], v[84:85], off offset:2064
	s_waitcnt vmcnt(0)
	s_branch .LBB0_1012
.LBB0_1011:
	s_or_b64 exec, exec, s[10:11]
	v_add_u32_e32 v0, 0x20000, v80
	v_ashrrev_i32_e32 v1, 31, v0
	v_readlane_b32 s10, v25, 0
	v_lshlrev_b64 v[0:1], 11, v[0:1]
	s_ashr_i32 s11, s10, 31
	global_load_dwordx4 v[52:55], v[90:91], off
	v_lshl_add_u64 v[0:1], v[86:87], 0, v[0:1]
	s_lshl_b64 s[10:11], s[10:11], 11
	global_load_dwordx4 v[48:51], v[0:1], off
	global_load_dwordx4 v[12:15], v[90:91], off offset:1024
	global_load_dwordx4 v[8:11], v[0:1], off offset:1024
	v_lshl_add_u64 v[0:1], v[86:87], 0, s[10:11]
	v_readlane_b32 s12, v25, 1
	global_load_dwordx4 v[56:59], v[0:1], off
	global_load_dwordx4 v[20:23], v[0:1], off offset:1024
	s_ashr_i32 s13, s12, 31
	v_readlane_b32 s14, v25, 2
	s_lshl_b64 s[12:13], s[12:13], 11
	s_ashr_i32 s15, s14, 31
	v_readlane_b32 s16, v25, 3
	v_lshl_add_u64 v[0:1], v[86:87], 0, s[12:13]
	s_lshl_b64 s[14:15], s[14:15], 11
	s_ashr_i32 s17, s16, 31
	v_readlane_b32 s18, v25, 4
	global_load_dwordx4 v[60:63], v[0:1], off
	global_load_dwordx4 v[28:31], v[0:1], off offset:1024
	v_lshl_add_u64 v[0:1], v[86:87], 0, s[14:15]
	s_lshl_b64 s[16:17], s[16:17], 11
	s_ashr_i32 s19, s18, 31
	global_load_dwordx4 v[68:71], v[0:1], off
	global_load_dwordx4 v[36:39], v[0:1], off offset:1024
	v_lshl_add_u64 v[0:1], v[86:87], 0, s[16:17]
	s_lshl_b64 s[18:19], s[18:19], 11
	global_load_dwordx4 v[72:75], v[0:1], off
	global_load_dwordx4 v[40:43], v[0:1], off offset:1024
	v_lshl_add_u64 v[0:1], v[86:87], 0, s[18:19]
	global_load_dwordx4 v[76:79], v[0:1], off
	global_load_dwordx4 v[44:47], v[0:1], off offset:1024
	v_readlane_b32 s20, v25, 5
	s_ashr_i32 s21, s20, 31
	v_readlane_b32 s22, v25, 6
	s_lshl_b64 s[20:21], s[20:21], 11
	s_ashr_i32 s23, s22, 31
	v_readlane_b32 s26, v25, 7
	v_lshl_add_u64 v[0:1], v[86:87], 0, s[20:21]
	s_lshl_b64 s[22:23], s[22:23], 11
	s_ashr_i32 s27, s26, 31
	global_load_dwordx4 v[16:19], v[0:1], off
	s_nop 0
	global_load_dwordx4 v[0:3], v[0:1], off offset:1024
	v_lshl_add_u64 v[4:5], v[86:87], 0, s[22:23]
	s_lshl_b64 s[26:27], s[26:27], 11
	s_waitcnt vmcnt(16)
	v_readlane_b32 s24, v24, 0
	v_readlane_b32 s10, v24, 1
	v_readlane_b32 s12, v24, 2
	v_readlane_b32 s14, v24, 3
	v_readlane_b32 s16, v24, 4
	v_readlane_b32 s18, v24, 5
	v_readlane_b32 s20, v24, 6
	global_load_dwordx4 v[32:35], v[4:5], off
	s_nop 0
	global_load_dwordx4 v[4:7], v[4:5], off offset:1024
	v_readlane_b32 s22, v24, 7
	v_lshl_add_u64 v[24:25], v[86:87], 0, s[26:27]
	global_load_dwordx4 v[64:67], v[24:25], off
	s_nop 0
	global_load_dwordx4 v[24:27], v[24:25], off offset:1024
	v_add_u32_e32 v80, s74, v80
	v_add_u32_e32 v88, s9, v88
	s_waitcnt vmcnt(19)
	v_lshlrev_b32_e32 v92, 16, v52
	v_and_b32_e32 v93, 0xffff0000, v52
	s_waitcnt vmcnt(18)
	v_lshlrev_b32_e32 v94, 16, v48
	v_and_b32_e32 v95, 0xffff0000, v48
	v_lshlrev_b32_e32 v52, 16, v53
	v_and_b32_e32 v53, 0xffff0000, v53
	v_lshlrev_b32_e32 v48, 16, v49
	v_and_b32_e32 v49, 0xffff0000, v49
	v_pk_fma_f32 v[48:49], v[52:53], s[8:9], v[48:49] op_sel_hi:[1,0,1]
	s_waitcnt vmcnt(15)
	v_lshlrev_b32_e32 v52, 16, v57
	v_and_b32_e32 v53, 0xffff0000, v57
	v_pk_fma_f32 v[102:103], s[24:25], v[52:53], v[48:49] op_sel_hi:[0,1,1]
	v_lshlrev_b32_e32 v48, 16, v54
	v_and_b32_e32 v49, 0xffff0000, v54
	v_lshlrev_b32_e32 v52, 16, v50
	v_and_b32_e32 v53, 0xffff0000, v50
	v_pk_fma_f32 v[48:49], v[48:49], s[8:9], v[52:53] op_sel_hi:[1,0,1]
	v_lshlrev_b32_e32 v52, 16, v58
	v_and_b32_e32 v53, 0xffff0000, v58
	v_pk_fma_f32 v[104:105], s[24:25], v[52:53], v[48:49] op_sel_hi:[0,1,1]
	v_lshlrev_b32_e32 v48, 16, v55
	v_and_b32_e32 v49, 0xffff0000, v55
	v_lshlrev_b32_e32 v50, 16, v51
	v_and_b32_e32 v51, 0xffff0000, v51
	v_pk_fma_f32 v[48:49], v[48:49], s[8:9], v[50:51] op_sel_hi:[1,0,1]
	v_lshlrev_b32_e32 v50, 16, v59
	v_and_b32_e32 v51, 0xffff0000, v59
	v_pk_fma_f32 v[58:59], s[24:25], v[50:51], v[48:49] op_sel_hi:[0,1,1]
	v_lshlrev_b32_e32 v48, 16, v12
	v_and_b32_e32 v49, 0xffff0000, v12
	v_lshlrev_b32_e32 v50, 16, v8
	v_and_b32_e32 v51, 0xffff0000, v8
	v_lshlrev_b32_e32 v12, 16, v13
	v_and_b32_e32 v13, 0xffff0000, v13
	v_lshlrev_b32_e32 v8, 16, v9
	v_and_b32_e32 v9, 0xffff0000, v9
	v_pk_fma_f32 v[48:49], v[48:49], s[8:9], v[50:51] op_sel_hi:[1,0,1]
	s_waitcnt vmcnt(14)
	v_lshlrev_b32_e32 v50, 16, v20
	v_and_b32_e32 v51, 0xffff0000, v20
	v_pk_fma_f32 v[8:9], v[12:13], s[8:9], v[8:9] op_sel_hi:[1,0,1]
	v_lshlrev_b32_e32 v12, 16, v21
	v_and_b32_e32 v13, 0xffff0000, v21
	v_pk_fma_f32 v[92:93], v[92:93], s[8:9], v[94:95] op_sel_hi:[1,0,1]
	v_lshlrev_b32_e32 v94, 16, v56
	v_and_b32_e32 v95, 0xffff0000, v56
	v_pk_fma_f32 v[48:49], s[24:25], v[50:51], v[48:49] op_sel_hi:[0,1,1]
	s_waitcnt vmcnt(12)
	v_lshlrev_b32_e32 v54, 16, v28
	v_and_b32_e32 v55, 0xffff0000, v28
	s_waitcnt vmcnt(10)
	v_lshlrev_b32_e32 v56, 16, v36
	v_and_b32_e32 v57, 0xffff0000, v36
	s_waitcnt vmcnt(8)
	v_lshlrev_b32_e32 v52, 16, v40
	v_and_b32_e32 v53, 0xffff0000, v40
	s_waitcnt vmcnt(6)
	v_lshlrev_b32_e32 v50, 16, v44
	v_and_b32_e32 v51, 0xffff0000, v44
	v_pk_fma_f32 v[8:9], s[24:25], v[12:13], v[8:9] op_sel_hi:[0,1,1]
	v_lshlrev_b32_e32 v12, 16, v29
	v_and_b32_e32 v13, 0xffff0000, v29
	v_lshlrev_b32_e32 v20, 16, v37
	v_and_b32_e32 v21, 0xffff0000, v37
	v_lshlrev_b32_e32 v28, 16, v41
	v_and_b32_e32 v29, 0xffff0000, v41
	v_lshlrev_b32_e32 v36, 16, v45
	v_and_b32_e32 v37, 0xffff0000, v45
	v_lshlrev_b32_e32 v40, 16, v14
	v_and_b32_e32 v41, 0xffff0000, v14
	v_lshlrev_b32_e32 v44, 16, v10
	v_and_b32_e32 v45, 0xffff0000, v10
	v_lshlrev_b32_e32 v14, 16, v15
	v_and_b32_e32 v15, 0xffff0000, v15
	v_lshlrev_b32_e32 v10, 16, v11
	v_and_b32_e32 v11, 0xffff0000, v11
	v_lshlrev_b32_e32 v106, 16, v62
	v_and_b32_e32 v107, 0xffff0000, v62
	v_lshlrev_b32_e32 v62, 16, v63
	v_and_b32_e32 v63, 0xffff0000, v63
	v_pk_fma_f32 v[40:41], v[40:41], s[8:9], v[44:45] op_sel_hi:[1,0,1]
	v_lshlrev_b32_e32 v44, 16, v22
	v_and_b32_e32 v45, 0xffff0000, v22
	v_pk_fma_f32 v[10:11], v[14:15], s[8:9], v[10:11] op_sel_hi:[1,0,1]
	v_lshlrev_b32_e32 v14, 16, v23
	v_and_b32_e32 v15, 0xffff0000, v23
	v_lshlrev_b32_e32 v108, 16, v70
	v_and_b32_e32 v109, 0xffff0000, v70
	v_lshlrev_b32_e32 v70, 16, v71
	v_and_b32_e32 v71, 0xffff0000, v71
	v_pk_fma_f32 v[40:41], s[24:25], v[44:45], v[40:41] op_sel_hi:[0,1,1]
	v_lshlrev_b32_e32 v44, 16, v30
	v_and_b32_e32 v45, 0xffff0000, v30
	v_lshlrev_b32_e32 v116, 16, v42
	v_and_b32_e32 v117, 0xffff0000, v42
	v_pk_fma_f32 v[10:11], s[24:25], v[14:15], v[10:11] op_sel_hi:[0,1,1]
	v_lshlrev_b32_e32 v14, 16, v31
	v_and_b32_e32 v15, 0xffff0000, v31
	v_lshlrev_b32_e32 v30, 16, v43
	v_and_b32_e32 v31, 0xffff0000, v43
	v_pk_fma_f32 v[42:43], s[10:11], v[62:63], v[58:59] op_sel_hi:[0,1,1]
	v_lshlrev_b32_e32 v110, 16, v74
	v_and_b32_e32 v111, 0xffff0000, v74
	v_lshlrev_b32_e32 v74, 16, v75
	v_and_b32_e32 v75, 0xffff0000, v75
	v_pk_fma_f32 v[42:43], s[12:13], v[70:71], v[42:43] op_sel_hi:[0,1,1]
	v_lshlrev_b32_e32 v112, 16, v78
	v_and_b32_e32 v113, 0xffff0000, v78
	v_lshlrev_b32_e32 v78, 16, v79
	v_and_b32_e32 v79, 0xffff0000, v79
	v_pk_fma_f32 v[42:43], s[14:15], v[74:75], v[42:43] op_sel_hi:[0,1,1]
	v_lshlrev_b32_e32 v114, 16, v38
	v_and_b32_e32 v115, 0xffff0000, v38
	v_lshlrev_b32_e32 v118, 16, v46
	v_and_b32_e32 v119, 0xffff0000, v46
	v_lshlrev_b32_e32 v22, 16, v39
	v_and_b32_e32 v23, 0xffff0000, v39
	v_lshlrev_b32_e32 v38, 16, v47
	v_and_b32_e32 v39, 0xffff0000, v47
	v_pk_fma_f32 v[42:43], s[16:17], v[78:79], v[42:43] op_sel_hi:[0,1,1]
	s_waitcnt vmcnt(5)
	v_lshlrev_b32_e32 v46, 16, v19
	v_and_b32_e32 v47, 0xffff0000, v19
	v_pk_fma_f32 v[42:43], s[18:19], v[46:47], v[42:43] op_sel_hi:[0,1,1]
	s_waitcnt vmcnt(3)
	v_lshlrev_b32_e32 v46, 16, v35
	v_and_b32_e32 v47, 0xffff0000, v35
	v_pk_fma_f32 v[42:43], s[20:21], v[46:47], v[42:43] op_sel_hi:[0,1,1]
	s_waitcnt vmcnt(1)
	v_lshlrev_b32_e32 v46, 16, v67
	v_and_b32_e32 v47, 0xffff0000, v67
	v_pk_fma_f32 v[42:43], s[22:23], v[46:47], v[42:43] op_sel_hi:[0,1,1]
	v_pk_fma_f32 v[46:47], s[10:11], v[106:107], v[104:105] op_sel_hi:[0,1,1]
	v_pk_fma_f32 v[46:47], s[12:13], v[108:109], v[46:47] op_sel_hi:[0,1,1]
	v_pk_fma_f32 v[46:47], s[14:15], v[110:111], v[46:47] op_sel_hi:[0,1,1]
	v_pk_fma_f32 v[10:11], s[10:11], v[14:15], v[10:11] op_sel_hi:[0,1,1]
	v_pk_fma_f32 v[46:47], s[16:17], v[112:113], v[46:47] op_sel_hi:[0,1,1]
	v_lshlrev_b32_e32 v58, 16, v18
	v_and_b32_e32 v59, 0xffff0000, v18
	v_pk_fma_f32 v[10:11], s[12:13], v[22:23], v[10:11] op_sel_hi:[0,1,1]
	v_pk_fma_f32 v[18:19], s[18:19], v[58:59], v[46:47] op_sel_hi:[0,1,1]
	v_lshlrev_b32_e32 v46, 16, v34
	v_and_b32_e32 v47, 0xffff0000, v34
	v_pk_fma_f32 v[10:11], s[14:15], v[30:31], v[10:11] op_sel_hi:[0,1,1]
	v_lshlrev_b32_e32 v100, 16, v60
	v_and_b32_e32 v101, 0xffff0000, v60
	v_lshlrev_b32_e32 v60, 16, v61
	v_and_b32_e32 v61, 0xffff0000, v61
	v_pk_fma_f32 v[18:19], s[20:21], v[46:47], v[18:19] op_sel_hi:[0,1,1]
	v_lshlrev_b32_e32 v34, 16, v66
	v_and_b32_e32 v35, 0xffff0000, v66
	v_pk_fma_f32 v[10:11], s[16:17], v[38:39], v[10:11] op_sel_hi:[0,1,1]
	v_lshlrev_b32_e32 v14, 16, v3
	v_and_b32_e32 v15, 0xffff0000, v3
	v_lshlrev_b32_e32 v98, 16, v68
	v_and_b32_e32 v99, 0xffff0000, v68
	v_lshlrev_b32_e32 v68, 16, v69
	v_and_b32_e32 v69, 0xffff0000, v69
	v_pk_fma_f32 v[18:19], s[22:23], v[34:35], v[18:19] op_sel_hi:[0,1,1]
	v_pk_fma_f32 v[34:35], s[10:11], v[60:61], v[102:103] op_sel_hi:[0,1,1]
	v_pk_fma_f32 v[10:11], s[18:19], v[14:15], v[10:11] op_sel_hi:[0,1,1]
	v_lshlrev_b32_e32 v14, 16, v7
	v_and_b32_e32 v15, 0xffff0000, v7
	v_pk_fma_f32 v[96:97], s[24:25], v[94:95], v[92:93] op_sel_hi:[0,1,1]
	v_lshlrev_b32_e32 v94, 16, v72
	v_and_b32_e32 v95, 0xffff0000, v72
	v_lshlrev_b32_e32 v72, 16, v73
	v_and_b32_e32 v73, 0xffff0000, v73
	v_pk_fma_f32 v[34:35], s[12:13], v[68:69], v[34:35] op_sel_hi:[0,1,1]
	v_pk_fma_f32 v[10:11], s[20:21], v[14:15], v[10:11] op_sel_hi:[0,1,1]
	s_waitcnt vmcnt(0)
	v_lshlrev_b32_e32 v14, 16, v27
	v_and_b32_e32 v15, 0xffff0000, v27
	v_lshlrev_b32_e32 v92, 16, v76
	v_and_b32_e32 v93, 0xffff0000, v76
	v_lshlrev_b32_e32 v76, 16, v77
	v_and_b32_e32 v77, 0xffff0000, v77
	v_pk_fma_f32 v[34:35], s[14:15], v[72:73], v[34:35] op_sel_hi:[0,1,1]
	v_pk_fma_f32 v[10:11], s[22:23], v[14:15], v[10:11] op_sel_hi:[0,1,1]
	v_pk_fma_f32 v[14:15], s[10:11], v[44:45], v[40:41] op_sel_hi:[0,1,1]
	v_pk_fma_f32 v[34:35], s[16:17], v[76:77], v[34:35] op_sel_hi:[0,1,1]
	v_lshlrev_b32_e32 v46, 16, v17
	v_and_b32_e32 v47, 0xffff0000, v17
	v_pk_fma_f32 v[14:15], s[12:13], v[114:115], v[14:15] op_sel_hi:[0,1,1]
	v_pk_fma_f32 v[34:35], s[18:19], v[46:47], v[34:35] op_sel_hi:[0,1,1]
	v_lshlrev_b32_e32 v46, 16, v33
	v_and_b32_e32 v47, 0xffff0000, v33
	v_pk_fma_f32 v[14:15], s[14:15], v[116:117], v[14:15] op_sel_hi:[0,1,1]
	v_pk_fma_f32 v[34:35], s[20:21], v[46:47], v[34:35] op_sel_hi:[0,1,1]
	v_lshlrev_b32_e32 v46, 16, v65
	v_and_b32_e32 v47, 0xffff0000, v65
	v_pk_fma_f32 v[14:15], s[16:17], v[118:119], v[14:15] op_sel_hi:[0,1,1]
	v_lshlrev_b32_e32 v22, 16, v2
	v_and_b32_e32 v23, 0xffff0000, v2
	v_pk_fma_f32 v[34:35], s[22:23], v[46:47], v[34:35] op_sel_hi:[0,1,1]
	v_pk_fma_f32 v[46:47], s[10:11], v[100:101], v[96:97] op_sel_hi:[0,1,1]
	v_pk_fma_f32 v[2:3], s[18:19], v[22:23], v[14:15] op_sel_hi:[0,1,1]
	v_lshlrev_b32_e32 v14, 16, v6
	v_and_b32_e32 v15, 0xffff0000, v6
	v_pk_fma_f32 v[46:47], s[12:13], v[98:99], v[46:47] op_sel_hi:[0,1,1]
	v_pk_fma_f32 v[2:3], s[20:21], v[14:15], v[2:3] op_sel_hi:[0,1,1]
	v_lshlrev_b32_e32 v6, 16, v26
	v_and_b32_e32 v7, 0xffff0000, v26
	v_pk_fma_f32 v[46:47], s[14:15], v[94:95], v[46:47] op_sel_hi:[0,1,1]
	v_pk_fma_f32 v[2:3], s[22:23], v[6:7], v[2:3] op_sel_hi:[0,1,1]
	v_pk_fma_f32 v[6:7], s[10:11], v[12:13], v[8:9] op_sel_hi:[0,1,1]
	v_pk_fma_f32 v[46:47], s[16:17], v[92:93], v[46:47] op_sel_hi:[0,1,1]
	v_lshlrev_b32_e32 v58, 16, v16
	v_and_b32_e32 v59, 0xffff0000, v16
	v_pk_fma_f32 v[6:7], s[12:13], v[20:21], v[6:7] op_sel_hi:[0,1,1]
	v_pk_fma_f32 v[16:17], s[18:19], v[58:59], v[46:47] op_sel_hi:[0,1,1]
	v_lshlrev_b32_e32 v46, 16, v32
	v_and_b32_e32 v47, 0xffff0000, v32
	v_pk_fma_f32 v[6:7], s[14:15], v[28:29], v[6:7] op_sel_hi:[0,1,1]
	v_pk_fma_f32 v[16:17], s[20:21], v[46:47], v[16:17] op_sel_hi:[0,1,1]
	v_lshlrev_b32_e32 v32, 16, v64
	v_and_b32_e32 v33, 0xffff0000, v64
	v_pk_fma_f32 v[6:7], s[16:17], v[36:37], v[6:7] op_sel_hi:[0,1,1]
	v_lshlrev_b32_e32 v8, 16, v1
	v_and_b32_e32 v9, 0xffff0000, v1
	v_pk_fma_f32 v[16:17], s[22:23], v[32:33], v[16:17] op_sel_hi:[0,1,1]
	v_pk_fma_f32 v[6:7], s[18:19], v[8:9], v[6:7] op_sel_hi:[0,1,1]
	v_lshlrev_b32_e32 v8, 16, v5
	v_and_b32_e32 v9, 0xffff0000, v5
	v_add_f32_e32 v32, 0, v16
	v_pk_fma_f32 v[6:7], s[20:21], v[8:9], v[6:7] op_sel_hi:[0,1,1]
	v_lshlrev_b32_e32 v8, 16, v25
	v_and_b32_e32 v9, 0xffff0000, v25
	v_add_f32_e32 v32, v17, v32
	v_pk_fma_f32 v[6:7], s[22:23], v[8:9], v[6:7] op_sel_hi:[0,1,1]
	v_pk_fma_f32 v[8:9], s[10:11], v[54:55], v[48:49] op_sel_hi:[0,1,1]
	v_add_f32_e32 v32, v34, v32
	v_pk_fma_f32 v[8:9], s[12:13], v[56:57], v[8:9] op_sel_hi:[0,1,1]
	v_add_f32_e32 v32, v35, v32
	v_pk_fma_f32 v[8:9], s[14:15], v[52:53], v[8:9] op_sel_hi:[0,1,1]
	v_add_f32_e32 v32, v18, v32
	v_pk_fma_f32 v[8:9], s[16:17], v[50:51], v[8:9] op_sel_hi:[0,1,1]
	v_lshlrev_b32_e32 v12, 16, v0
	v_and_b32_e32 v13, 0xffff0000, v0
	v_add_f32_e32 v32, v19, v32
	v_pk_fma_f32 v[0:1], s[18:19], v[12:13], v[8:9] op_sel_hi:[0,1,1]
	v_lshlrev_b32_e32 v8, 16, v4
	v_and_b32_e32 v9, 0xffff0000, v4
	v_add_f32_e32 v32, v42, v32
	v_pk_fma_f32 v[0:1], s[20:21], v[8:9], v[0:1] op_sel_hi:[0,1,1]
	v_lshlrev_b32_e32 v4, 16, v24
	v_and_b32_e32 v5, 0xffff0000, v24
	v_add_f32_e32 v32, v43, v32
	v_pk_fma_f32 v[0:1], s[22:23], v[4:5], v[0:1] op_sel_hi:[0,1,1]
	v_add_f32_e32 v4, v0, v32
	v_add_f32_e32 v4, v1, v4
	v_add_f32_e32 v4, v6, v4
	v_add_f32_e32 v4, v7, v4
	v_add_f32_e32 v4, v2, v4
	v_add_f32_e32 v4, v3, v4
	v_add_f32_e32 v4, v10, v4
	v_add_f32_e32 v4, v11, v4
	s_mov_b32 s10, 0x800000
	s_nop 0
	v_add_f32_dpp v4, v4, v4 quad_perm:[1,0,3,2] row_mask:0xf bank_mask:0xf bound_ctrl:1
	s_nop 1
	v_add_f32_dpp v4, v4, v4 quad_perm:[2,3,0,1] row_mask:0xf bank_mask:0xf bound_ctrl:1
	s_nop 1
	v_add_f32_dpp v4, v4, v4 row_half_mirror row_mask:0xf bank_mask:0xf bound_ctrl:1
	s_nop 1
	v_add_f32_dpp v4, v4, v4 row_mirror row_mask:0xf bank_mask:0xf bound_ctrl:1
	v_mov_b32_e32 v5, v4
	s_nop 1
	v_permlane16_swap_b32 v5, v4
	s_nop 0
	v_add_f32_e32 v4, v5, v4
	v_mov_b32_e32 v5, v4
	s_nop 1
	v_permlane32_swap_b32 v4, v5
	s_nop 0
	v_add_f32_e32 v4, v4, v5
	v_mul_f32_e32 v4, 0x3a800000, v4
	v_pk_add_f32 v[26:27], v[16:17], v[4:5] op_sel_hi:[1,0] neg_lo:[0,1] neg_hi:[0,1]
	v_pk_add_f32 v[28:29], v[34:35], v[4:5] op_sel_hi:[1,0] neg_lo:[0,1] neg_hi:[0,1]
	v_pk_mul_f32 v[8:9], v[26:27], v[26:27]
	v_pk_mul_f32 v[12:13], v[28:29], v[28:29]
	v_add_f32_e32 v8, v8, v9
	v_pk_add_f32 v[30:31], v[18:19], v[4:5] op_sel_hi:[1,0] neg_lo:[0,1] neg_hi:[0,1]
	v_add_f32_e32 v8, v12, v8
	v_pk_mul_f32 v[14:15], v[30:31], v[30:31]
	v_add_f32_e32 v8, v13, v8
	v_pk_add_f32 v[32:33], v[42:43], v[4:5] op_sel_hi:[1,0] neg_lo:[0,1] neg_hi:[0,1]
	v_add_f32_e32 v8, v14, v8
	v_pk_mul_f32 v[24:25], v[32:33], v[32:33]
	v_add_f32_e32 v8, v15, v8
	v_pk_add_f32 v[16:17], v[0:1], v[4:5] op_sel_hi:[1,0] neg_lo:[0,1] neg_hi:[0,1]
	v_add_f32_e32 v8, v24, v8
	v_pk_mul_f32 v[0:1], v[16:17], v[16:17]
	v_add_f32_e32 v8, v25, v8
	v_pk_add_f32 v[18:19], v[6:7], v[4:5] op_sel_hi:[1,0] neg_lo:[0,1] neg_hi:[0,1]
	v_add_f32_e32 v0, v0, v8
	v_pk_mul_f32 v[6:7], v[18:19], v[18:19]
	v_add_f32_e32 v0, v1, v0
	v_pk_add_f32 v[20:21], v[2:3], v[4:5] op_sel_hi:[1,0] neg_lo:[0,1] neg_hi:[0,1]
	v_add_f32_e32 v0, v6, v0
	v_pk_mul_f32 v[2:3], v[20:21], v[20:21]
	v_add_f32_e32 v0, v7, v0
	v_pk_add_f32 v[22:23], v[10:11], v[4:5] op_sel_hi:[1,0] neg_lo:[0,1] neg_hi:[0,1]
	v_add_f32_e32 v0, v2, v0
	v_pk_mul_f32 v[4:5], v[22:23], v[22:23]
	v_add_f32_e32 v0, v3, v0
	v_add_f32_e32 v0, v4, v0
	v_add_f32_e32 v0, v5, v0
	s_nop 1
	v_add_f32_dpp v0, v0, v0 quad_perm:[1,0,3,2] row_mask:0xf bank_mask:0xf bound_ctrl:1
	s_nop 1
	v_add_f32_dpp v0, v0, v0 quad_perm:[2,3,0,1] row_mask:0xf bank_mask:0xf bound_ctrl:1
	s_nop 1
	v_add_f32_dpp v0, v0, v0 row_half_mirror row_mask:0xf bank_mask:0xf bound_ctrl:1
	s_nop 1
	v_add_f32_dpp v0, v0, v0 row_mirror row_mask:0xf bank_mask:0xf bound_ctrl:1
	v_mov_b32_e32 v1, v0
	s_nop 1
	v_permlane16_swap_b32 v1, v0
	s_nop 0
	v_add_f32_e32 v0, v1, v0
	v_mov_b32_e32 v1, v0
	s_nop 1
	v_permlane32_swap_b32 v1, v0
	s_nop 0
	v_add_f32_e32 v0, v1, v0
	v_fmamk_f32 v0, v0, 0x3a800000, v81
	v_cmp_gt_f32_e32 vcc, s10, v0
	v_mul_f32_e32 v1, 0x4b800000, v0
	s_mov_b32 s10, 0xf2b00000
	v_cndmask_b32_e32 v0, v0, v1, vcc
	v_rsq_f32_e32 v0, v0
	s_nop 0
	v_mul_f32_e32 v1, 0x45800000, v0
	v_cndmask_b32_e32 v24, v0, v1, vcc
	v_pk_mul_f32 v[26:27], v[26:27], v[24:25] op_sel_hi:[1,0]
	v_pk_mul_f32 v[16:17], v[16:17], v[24:25] op_sel_hi:[1,0]
	v_pk_fma_f32 v[8:9], v[200:201], v[26:27], v[208:209]
	v_pk_mul_f32 v[12:13], v[28:29], v[24:25] op_sel_hi:[1,0]
	s_nop 0
	v_pk_fma_f32 v[10:11], v[202:203], v[12:13], v[210:211]
	v_pk_mul_f32 v[12:13], v[30:31], v[24:25] op_sel_hi:[1,0]
	s_nop 0
	v_pk_fma_f32 v[4:5], v[204:205], v[12:13], v[212:213]
	v_pk_mul_f32 v[0:1], v[32:33], v[24:25] op_sel_hi:[1,0]
	s_nop 0
	v_pk_fma_f32 v[6:7], v[0:1], v[206:207], v[214:215]
	v_cvt_pk_bf16_f32 v2, v4, v5
	v_add_co_u32_e32 v4, vcc, s10, v90
	v_cvt_pk_bf16_f32 v0, v8, v9
	v_cvt_pk_bf16_f32 v1, v10, v11
	v_cvt_pk_bf16_f32 v3, v6, v7
	v_addc_co_u32_e32 v5, vcc, -1, v91, vcc
	global_store_dwordx4 v[4:5], v[0:3], off
	s_movk_i32 s10, 0x3fff
	v_pk_fma_f32 v[4:5], v[16:17], v[216:217], v[224:225]
	v_pk_mul_f32 v[12:13], v[18:19], v[24:25] op_sel_hi:[1,0]
	s_nop 0
	v_pk_fma_f32 v[6:7], v[12:13], v[218:219], v[226:227]
	v_pk_mul_f32 v[12:13], v[20:21], v[24:25] op_sel_hi:[1,0]
	s_nop 0
	v_pk_fma_f32 v[8:9], v[12:13], v[220:221], v[228:229]
	v_pk_mul_f32 v[0:1], v[22:23], v[24:25] op_sel_hi:[1,0]
	s_nop 0
	v_pk_fma_f32 v[10:11], v[0:1], v[222:223], v[230:231]
	v_cvt_pk_bf16_f32 v0, v4, v5
	v_add_co_u32_e32 v4, vcc, 0xf2b01000, v90
	v_cvt_pk_bf16_f32 v1, v6, v7
	s_nop 0
	v_addc_co_u32_e32 v5, vcc, -1, v91, vcc
	v_cmp_lt_i32_e32 vcc, s10, v80
	v_cvt_pk_bf16_f32 v2, v8, v9
	v_cvt_pk_bf16_f32 v3, v10, v11
	v_lshl_add_u64 v[90:91], v[90:91], 0, s[4:5]
	s_or_b64 s[6:7], vcc, s[6:7]
	global_store_dwordx4 v[4:5], v[0:3], off offset:-3072
	s_andn2_b64 exec, exec, s[6:7]
	s_cbranch_execz .LBB0_1014

.LBB0_2588:
	s_or_b64 exec, exec, s[0:1]
	v_ashrrev_i32_e32 v0, 6, v3
	v_readlane_b32 s0, v253, 30
	s_waitcnt lgkmcnt(0)
	s_barrier
	v_add_u32_e32 v24, s0, v0
	s_movk_i32 s0, 0x4000
	v_cmp_gt_i32_e32 vcc, s0, v24
	s_and_saveexec_b64 s[0:1], vcc
	s_cbranch_execz .LBB0_2595
	v_readlane_b32 s0, v253, 4
	v_readlane_b32 s2, v253, 6
	v_readlane_b32 s14, v253, 18
	v_readlane_b32 s3, v253, 7
	v_readlane_b32 s15, v253, 19
	s_add_u32 s2, s14, 0x1000
	v_and_b32_e32 v1, 63, v2
	v_readlane_b32 s6, v253, 10
	s_addc_u32 s3, s15, 0
	v_lshlrev_b32_e32 v2, 5, v1
	v_mov_b32_e32 v3, 0
	v_readlane_b32 s7, v253, 11
	s_add_u32 s6, s64, 0x1000
	v_or_b32_e32 v4, 0x800, v2
	v_mov_b32_e32 v5, v3
	s_addc_u32 s7, s65, 0
	v_lshl_add_u64 v[26:27], s[2:3], 0, v[2:3]
	v_lshl_add_u64 v[30:31], s[2:3], 0, v[4:5]
	v_readlane_b32 s2, v254, 3
	v_readlane_b32 s12, v253, 16
	v_readlane_b32 s13, v253, 17
	s_cmp_lg_u64 s[66:67], 0
	v_lshl_add_u64 v[32:33], s[6:7], 0, v[4:5]
	v_lshlrev_b32_e32 v4, 4, v1
	v_readlane_b32 s3, v254, 4
	v_readlane_b32 s1, v253, 5
	s_cselect_b64 s[12:13], -1, 0
	v_lshl_add_u64 v[34:35], s[2:3], 0, v[4:5]
	s_lshl_b32 s2, s72, 6
	v_lshlrev_b32_e32 v0, 3, v0
	v_ashrrev_i32_e32 v25, 31, v24
	v_cmp_gt_u32_e64 s[0:1], 8, v1
	v_add3_u32 v36, s2, v0, v1
	v_readlane_b32 s2, v253, 2
	v_lshlrev_b64 v[0:1], 11, v[24:25]
	v_readlane_b32 s11, v253, 15
	v_readlane_b32 s3, v253, 3
	v_or_b32_e32 v0, v0, v4
	s_lshl_b32 s11, s2, 6
	v_lshl_add_u64 v[0:1], s[70:71], 0, v[0:1]
	s_mov_b64 s[2:3], 0xd60d900
	v_lshl_add_u64 v[38:39], v[0:1], 0, s[2:3]
	v_lshlrev_b64 v[0:1], 12, v[24:25]
	v_or_b32_e32 v0, v0, v2
	v_lshl_add_u64 v[0:1], s[66:67], 0, v[0:1]
	s_mov_b64 s[2:3], 0x800
	v_readlane_b32 s4, v253, 8
	v_readlane_b32 s5, v253, 9
	v_readlane_b32 s8, v253, 12
	v_readlane_b32 s9, v253, 13
	v_readlane_b32 s10, v253, 14
	s_ashr_i32 s75, s74, 31
	v_lshl_add_u64 v[40:41], v[0:1], 0, s[2:3]
	v_cndmask_b32_e64 v0, 0, 1, s[12:13]
	s_mov_b64 s[4:5], 0
	v_lshl_add_u64 v[28:29], s[6:7], 0, v[2:3]
	s_lshl_b64 s[6:7], s[74:75], 11
	s_lshl_b64 s[8:9], s[74:75], 12
	s_mov_b32 s10, 0x3fb504f3
	v_mov_b32_e32 v25, 0x3727c5ac
	s_mov_b32 s15, 0x800000
	s_movk_i32 s17, 0x3fff
	v_cmp_ne_u32_e64 s[2:3], 1, v0
	global_load_dwordx4 v[200:203], v[26:27], off
	global_load_dwordx4 v[204:207], v[28:29], off
	global_load_dwordx4 v[208:211], v[26:27], off offset:16
	global_load_dwordx4 v[212:215], v[28:29], off offset:16
	global_load_dwordx4 v[216:219], v[30:31], off
	global_load_dwordx4 v[220:223], v[32:33], off
	global_load_dwordx4 v[224:227], v[30:31], off offset:16
	global_load_dwordx4 v[228:231], v[32:33], off offset:16
	s_waitcnt vmcnt(0)
	s_branch .LBB0_2591

.LBB0_2593:
	s_or_b64 exec, exec, s[12:13]
	v_readlane_b32 s12, v1, 0
	s_ashr_i32 s13, s12, 31
	s_lshl_b64 s[12:13], s[12:13], 11
	v_lshl_add_u64 v[98:99], v[34:35], 0, s[12:13]
	v_readlane_b32 s12, v1, 1
	s_ashr_i32 s13, s12, 31
	s_lshl_b64 s[12:13], s[12:13], 11
	v_lshl_add_u64 v[100:101], v[34:35], 0, s[12:13]
	v_readlane_b32 s12, v1, 2
	s_ashr_i32 s13, s12, 31
	s_lshl_b64 s[12:13], s[12:13], 11
	v_add_u32_e32 v2, 0x20000, v24
	v_lshl_add_u64 v[102:103], v[34:35], 0, s[12:13]
	v_readlane_b32 s12, v1, 3
	v_ashrrev_i32_e32 v3, 31, v2
	s_ashr_i32 s13, s12, 31
	v_lshlrev_b64 v[2:3], 11, v[2:3]
	s_lshl_b64 s[12:13], s[12:13], 11
	v_lshl_add_u64 v[2:3], v[34:35], 0, v[2:3]
	v_lshl_add_u64 v[104:105], v[34:35], 0, s[12:13]
	v_readlane_b32 s12, v1, 4
	global_load_dwordx4 v[42:45], v[38:39], off offset:-1024
	global_load_dwordx4 v[46:49], v[2:3], off
	s_ashr_i32 s13, s12, 31
	global_load_dwordx4 v[50:53], v[98:99], off
	global_load_dwordx4 v[54:57], v[100:101], off
	s_lshl_b64 s[12:13], s[12:13], 11
	global_load_dwordx4 v[58:61], v[102:103], off
	global_load_dwordx4 v[62:65], v[104:105], off
	v_lshl_add_u64 v[106:107], v[34:35], 0, s[12:13]
	global_load_dwordx4 v[66:69], v[106:107], off
	global_load_dwordx4 v[70:73], v[38:39], off
	global_load_dwordx4 v[74:77], v[2:3], off offset:1024
	v_readlane_b32 s28, v1, 5
	v_readlane_b32 s30, v1, 6
	v_readlane_b32 s34, v1, 7
	s_ashr_i32 s29, s28, 31
	s_ashr_i32 s31, s30, 31
	s_ashr_i32 s35, s34, 31
	s_lshl_b64 s[28:29], s[28:29], 11
	s_lshl_b64 s[30:31], s[30:31], 11
	s_lshl_b64 s[34:35], s[34:35], 11
	s_waitcnt vmcnt(9)
	v_readlane_b32 s26, v0, 0
	v_readlane_b32 s22, v0, 1
	v_readlane_b32 s20, v0, 2
	v_readlane_b32 s16, v0, 3
	v_readlane_b32 s14, v0, 4
	v_readlane_b32 s12, v0, 5
	v_readlane_b32 s18, v0, 6
	v_readlane_b32 s24, v0, 7
	v_lshl_add_u64 v[108:109], v[34:35], 0, s[28:29]
	v_lshl_add_u64 v[110:111], v[34:35], 0, s[30:31]
	v_lshl_add_u64 v[112:113], v[34:35], 0, s[34:35]
	global_load_dwordx4 v[78:81], v[98:99], off offset:1024
	global_load_dwordx4 v[82:85], v[100:101], off offset:1024
	global_load_dwordx4 v[86:89], v[102:103], off offset:1024
	global_load_dwordx4 v[90:93], v[104:105], off offset:1024
	global_load_dwordx4 v[94:97], v[106:107], off offset:1024
	global_load_dwordx4 v[20:23], v[108:109], off
	global_load_dwordx4 v[8:11], v[108:109], off offset:1024
	global_load_dwordx4 v[16:19], v[110:111], off
	global_load_dwordx4 v[4:7], v[110:111], off offset:1024
	global_load_dwordx4 v[12:15], v[112:113], off
	global_load_dwordx4 v[0:3], v[112:113], off offset:1024
	s_and_b64 vcc, exec, s[2:3]
	s_waitcnt vmcnt(19)
	v_lshlrev_b32_e32 v98, 16, v42
	v_and_b32_e32 v99, 0xffff0000, v42
	v_lshlrev_b32_e32 v42, 16, v43
	v_and_b32_e32 v43, 0xffff0000, v43
	s_waitcnt vmcnt(18)
	v_lshlrev_b32_e32 v100, 16, v46
	v_and_b32_e32 v101, 0xffff0000, v46
	v_lshlrev_b32_e32 v46, 16, v47
	v_and_b32_e32 v47, 0xffff0000, v47
	s_waitcnt vmcnt(17)
	v_lshlrev_b32_e32 v102, 16, v50
	v_and_b32_e32 v103, 0xffff0000, v50
	v_lshlrev_b32_e32 v50, 16, v51
	v_and_b32_e32 v51, 0xffff0000, v51
	v_pk_fma_f32 v[98:99], v[98:99], s[10:11], v[100:101] op_sel_hi:[1,0,1]
	v_pk_fma_f32 v[42:43], v[42:43], s[10:11], v[46:47] op_sel_hi:[1,0,1]
	s_waitcnt vmcnt(16)
	v_lshlrev_b32_e32 v104, 16, v54
	v_and_b32_e32 v105, 0xffff0000, v54
	s_waitcnt vmcnt(15)
	v_lshlrev_b32_e32 v106, 16, v58
	v_and_b32_e32 v107, 0xffff0000, v58
	s_waitcnt vmcnt(14)
	v_lshlrev_b32_e32 v108, 16, v62
	v_and_b32_e32 v109, 0xffff0000, v62
	s_waitcnt vmcnt(13)
	v_lshlrev_b32_e32 v110, 16, v66
	v_and_b32_e32 v111, 0xffff0000, v66
	v_pk_fma_f32 v[46:47], s[26:27], v[102:103], v[98:99] op_sel_hi:[0,1,1]
	v_pk_fma_f32 v[42:43], s[26:27], v[50:51], v[42:43] op_sel_hi:[0,1,1]
	v_lshlrev_b32_e32 v50, 16, v55
	v_and_b32_e32 v51, 0xffff0000, v55
	v_lshlrev_b32_e32 v54, 16, v59
	v_and_b32_e32 v55, 0xffff0000, v59
	v_lshlrev_b32_e32 v58, 16, v63
	v_and_b32_e32 v59, 0xffff0000, v63
	v_lshlrev_b32_e32 v62, 16, v67
	v_and_b32_e32 v63, 0xffff0000, v67
	v_lshlrev_b32_e32 v66, 16, v44
	v_and_b32_e32 v67, 0xffff0000, v44
	v_lshlrev_b32_e32 v98, 16, v48
	v_and_b32_e32 v99, 0xffff0000, v48
	v_lshlrev_b32_e32 v44, 16, v45
	v_and_b32_e32 v45, 0xffff0000, v45
	v_lshlrev_b32_e32 v48, 16, v49
	v_and_b32_e32 v49, 0xffff0000, v49
	v_pk_fma_f32 v[66:67], v[66:67], s[10:11], v[98:99] op_sel_hi:[1,0,1]
	v_lshlrev_b32_e32 v98, 16, v52
	v_and_b32_e32 v99, 0xffff0000, v52
	v_pk_fma_f32 v[44:45], v[44:45], s[10:11], v[48:49] op_sel_hi:[1,0,1]
	v_lshlrev_b32_e32 v48, 16, v53
	v_and_b32_e32 v49, 0xffff0000, v53
	v_pk_fma_f32 v[66:67], s[26:27], v[98:99], v[66:67] op_sel_hi:[0,1,1]
	v_lshlrev_b32_e32 v98, 16, v56
	v_and_b32_e32 v99, 0xffff0000, v56
	v_lshlrev_b32_e32 v100, 16, v60
	v_and_b32_e32 v101, 0xffff0000, v60
	v_lshlrev_b32_e32 v102, 16, v64
	v_and_b32_e32 v103, 0xffff0000, v64
	v_lshlrev_b32_e32 v112, 16, v68
	v_and_b32_e32 v113, 0xffff0000, v68
	v_pk_fma_f32 v[44:45], s[26:27], v[48:49], v[44:45] op_sel_hi:[0,1,1]
	v_lshlrev_b32_e32 v48, 16, v57
	v_and_b32_e32 v49, 0xffff0000, v57
	v_lshlrev_b32_e32 v52, 16, v61
	v_and_b32_e32 v53, 0xffff0000, v61
	v_lshlrev_b32_e32 v56, 16, v65
	v_and_b32_e32 v57, 0xffff0000, v65
	v_lshlrev_b32_e32 v60, 16, v69
	v_and_b32_e32 v61, 0xffff0000, v69
	s_waitcnt vmcnt(12)
	v_lshlrev_b32_e32 v64, 16, v70
	v_and_b32_e32 v65, 0xffff0000, v70
	s_waitcnt vmcnt(11)
	v_lshlrev_b32_e32 v68, 16, v74
	v_and_b32_e32 v69, 0xffff0000, v74
	v_lshlrev_b32_e32 v70, 16, v71
	v_and_b32_e32 v71, 0xffff0000, v71
	v_lshlrev_b32_e32 v74, 16, v75
	v_and_b32_e32 v75, 0xffff0000, v75
	v_pk_fma_f32 v[64:65], v[64:65], s[10:11], v[68:69] op_sel_hi:[1,0,1]
	s_waitcnt vmcnt(10)
	v_lshlrev_b32_e32 v68, 16, v78
	v_and_b32_e32 v69, 0xffff0000, v78
	v_pk_fma_f32 v[70:71], v[70:71], s[10:11], v[74:75] op_sel_hi:[1,0,1]
	v_lshlrev_b32_e32 v74, 16, v79
	v_and_b32_e32 v75, 0xffff0000, v79
	v_pk_fma_f32 v[46:47], s[22:23], v[104:105], v[46:47] op_sel_hi:[0,1,1]
	v_pk_fma_f32 v[64:65], s[26:27], v[68:69], v[64:65] op_sel_hi:[0,1,1]
	s_waitcnt vmcnt(9)
	v_lshlrev_b32_e32 v68, 16, v82
	v_and_b32_e32 v69, 0xffff0000, v82
	s_waitcnt vmcnt(8)
	v_lshlrev_b32_e32 v114, 16, v86
	v_and_b32_e32 v115, 0xffff0000, v86
	s_waitcnt vmcnt(7)
	v_lshlrev_b32_e32 v116, 16, v90
	v_and_b32_e32 v117, 0xffff0000, v90
	s_waitcnt vmcnt(6)
	v_lshlrev_b32_e32 v118, 16, v94
	v_and_b32_e32 v119, 0xffff0000, v94
	v_pk_fma_f32 v[70:71], s[26:27], v[74:75], v[70:71] op_sel_hi:[0,1,1]
	v_lshlrev_b32_e32 v74, 16, v83
	v_and_b32_e32 v75, 0xffff0000, v83
	v_lshlrev_b32_e32 v78, 16, v87
	v_and_b32_e32 v79, 0xffff0000, v87
	v_lshlrev_b32_e32 v82, 16, v91
	v_and_b32_e32 v83, 0xffff0000, v91
	v_lshlrev_b32_e32 v86, 16, v95
	v_and_b32_e32 v87, 0xffff0000, v95
	v_lshlrev_b32_e32 v90, 16, v72
	v_and_b32_e32 v91, 0xffff0000, v72
	v_lshlrev_b32_e32 v94, 16, v76
	v_and_b32_e32 v95, 0xffff0000, v76
	v_lshlrev_b32_e32 v72, 16, v73
	v_and_b32_e32 v73, 0xffff0000, v73
	v_lshlrev_b32_e32 v76, 16, v77
	v_and_b32_e32 v77, 0xffff0000, v77
	v_pk_fma_f32 v[46:47], s[20:21], v[106:107], v[46:47] op_sel_hi:[0,1,1]
	v_pk_fma_f32 v[90:91], v[90:91], s[10:11], v[94:95] op_sel_hi:[1,0,1]
	v_lshlrev_b32_e32 v94, 16, v80
	v_and_b32_e32 v95, 0xffff0000, v80
	v_pk_fma_f32 v[72:73], v[72:73], s[10:11], v[76:77] op_sel_hi:[1,0,1]
	v_lshlrev_b32_e32 v76, 16, v81
	v_and_b32_e32 v77, 0xffff0000, v81
	v_pk_fma_f32 v[46:47], s[16:17], v[108:109], v[46:47] op_sel_hi:[0,1,1]
	v_pk_fma_f32 v[90:91], s[26:27], v[94:95], v[90:91] op_sel_hi:[0,1,1]
	v_lshlrev_b32_e32 v94, 16, v84
	v_and_b32_e32 v95, 0xffff0000, v84
	v_lshlrev_b32_e32 v122, 16, v92
	v_and_b32_e32 v123, 0xffff0000, v92
	v_pk_fma_f32 v[72:73], s[26:27], v[76:77], v[72:73] op_sel_hi:[0,1,1]
	v_lshlrev_b32_e32 v76, 16, v85
	v_and_b32_e32 v77, 0xffff0000, v85
	v_lshlrev_b32_e32 v84, 16, v93
	v_and_b32_e32 v85, 0xffff0000, v93
	v_pk_fma_f32 v[46:47], s[14:15], v[110:111], v[46:47] op_sel_hi:[0,1,1]
	s_waitcnt vmcnt(5)
	v_lshlrev_b32_e32 v92, 16, v20
	v_and_b32_e32 v93, 0xffff0000, v20
	v_pk_fma_f32 v[42:43], s[22:23], v[50:51], v[42:43] op_sel_hi:[0,1,1]
	v_pk_fma_f32 v[46:47], s[12:13], v[92:93], v[46:47] op_sel_hi:[0,1,1]
	s_waitcnt vmcnt(3)
	v_lshlrev_b32_e32 v92, 16, v16
	v_and_b32_e32 v93, 0xffff0000, v16
	v_pk_fma_f32 v[42:43], s[20:21], v[54:55], v[42:43] op_sel_hi:[0,1,1]
	v_pk_fma_f32 v[46:47], s[18:19], v[92:93], v[46:47] op_sel_hi:[0,1,1]
	s_waitcnt vmcnt(1)
	v_lshlrev_b32_e32 v92, 16, v12
	v_and_b32_e32 v93, 0xffff0000, v12
	v_pk_fma_f32 v[42:43], s[16:17], v[58:59], v[42:43] op_sel_hi:[0,1,1]
	v_pk_fma_f32 v[46:47], s[24:25], v[92:93], v[46:47] op_sel_hi:[0,1,1]
	v_pk_fma_f32 v[42:43], s[14:15], v[62:63], v[42:43] op_sel_hi:[0,1,1]
	v_lshlrev_b32_e32 v20, 16, v21
	v_and_b32_e32 v21, 0xffff0000, v21
	v_add_f32_e32 v12, 0, v46
	v_pk_fma_f32 v[20:21], s[12:13], v[20:21], v[42:43] op_sel_hi:[0,1,1]
	v_lshlrev_b32_e32 v16, 16, v17
	v_and_b32_e32 v17, 0xffff0000, v17
	v_add_f32_e32 v37, v47, v12
	v_pk_fma_f32 v[16:17], s[18:19], v[16:17], v[20:21] op_sel_hi:[0,1,1]
	v_lshlrev_b32_e32 v12, 16, v13
	v_and_b32_e32 v13, 0xffff0000, v13
	v_pk_fma_f32 v[16:17], s[24:25], v[12:13], v[16:17] op_sel_hi:[0,1,1]
	v_add_f32_e32 v12, v16, v37
	v_add_f32_e32 v37, v17, v12
	v_pk_fma_f32 v[12:13], s[22:23], v[98:99], v[66:67] op_sel_hi:[0,1,1]
	v_pk_fma_f32 v[12:13], s[20:21], v[100:101], v[12:13] op_sel_hi:[0,1,1]
	v_pk_fma_f32 v[12:13], s[16:17], v[102:103], v[12:13] op_sel_hi:[0,1,1]
	v_pk_fma_f32 v[12:13], s[14:15], v[112:113], v[12:13] op_sel_hi:[0,1,1]
	v_lshlrev_b32_e32 v20, 16, v22
	v_and_b32_e32 v21, 0xffff0000, v22
	v_pk_fma_f32 v[12:13], s[12:13], v[20:21], v[12:13] op_sel_hi:[0,1,1]
	v_lshlrev_b32_e32 v20, 16, v18
	v_and_b32_e32 v21, 0xffff0000, v18
	v_pk_fma_f32 v[12:13], s[18:19], v[20:21], v[12:13] op_sel_hi:[0,1,1]
	v_lshlrev_b32_e32 v20, 16, v14
	v_and_b32_e32 v21, 0xffff0000, v14
	v_pk_fma_f32 v[20:21], s[24:25], v[20:21], v[12:13] op_sel_hi:[0,1,1]
	v_add_f32_e32 v12, v20, v37
	v_add_f32_e32 v37, v21, v12
	v_pk_fma_f32 v[12:13], s[22:23], v[48:49], v[44:45] op_sel_hi:[0,1,1]
	v_pk_fma_f32 v[12:13], s[20:21], v[52:53], v[12:13] op_sel_hi:[0,1,1]
	v_pk_fma_f32 v[12:13], s[16:17], v[56:57], v[12:13] op_sel_hi:[0,1,1]
	v_pk_fma_f32 v[12:13], s[14:15], v[60:61], v[12:13] op_sel_hi:[0,1,1]
	v_lshlrev_b32_e32 v22, 16, v23
	v_and_b32_e32 v23, 0xffff0000, v23
	v_pk_fma_f32 v[12:13], s[12:13], v[22:23], v[12:13] op_sel_hi:[0,1,1]
	v_lshlrev_b32_e32 v18, 16, v19
	v_and_b32_e32 v19, 0xffff0000, v19
	v_pk_fma_f32 v[12:13], s[18:19], v[18:19], v[12:13] op_sel_hi:[0,1,1]
	v_lshlrev_b32_e32 v14, 16, v15
	v_and_b32_e32 v15, 0xffff0000, v15
	v_pk_fma_f32 v[18:19], s[24:25], v[14:15], v[12:13] op_sel_hi:[0,1,1]
	v_add_f32_e32 v12, v18, v37
	v_add_f32_e32 v37, v19, v12
	v_pk_fma_f32 v[12:13], s[22:23], v[68:69], v[64:65] op_sel_hi:[0,1,1]
	v_pk_fma_f32 v[12:13], s[20:21], v[114:115], v[12:13] op_sel_hi:[0,1,1]
	v_pk_fma_f32 v[12:13], s[16:17], v[116:117], v[12:13] op_sel_hi:[0,1,1]
	v_pk_fma_f32 v[12:13], s[14:15], v[118:119], v[12:13] op_sel_hi:[0,1,1]
	v_lshlrev_b32_e32 v14, 16, v8
	v_and_b32_e32 v15, 0xffff0000, v8
	v_pk_fma_f32 v[12:13], s[12:13], v[14:15], v[12:13] op_sel_hi:[0,1,1]
	v_lshlrev_b32_e32 v14, 16, v4
	v_and_b32_e32 v15, 0xffff0000, v4
	v_pk_fma_f32 v[12:13], s[18:19], v[14:15], v[12:13] op_sel_hi:[0,1,1]
	s_waitcnt vmcnt(0)
	v_lshlrev_b32_e32 v14, 16, v0
	v_and_b32_e32 v15, 0xffff0000, v0
	v_pk_fma_f32 v[22:23], s[24:25], v[14:15], v[12:13] op_sel_hi:[0,1,1]
	v_pk_fma_f32 v[12:13], s[22:23], v[74:75], v[70:71] op_sel_hi:[0,1,1]
	v_pk_fma_f32 v[12:13], s[20:21], v[78:79], v[12:13] op_sel_hi:[0,1,1]
	v_pk_fma_f32 v[12:13], s[16:17], v[82:83], v[12:13] op_sel_hi:[0,1,1]
	v_pk_fma_f32 v[12:13], s[14:15], v[86:87], v[12:13] op_sel_hi:[0,1,1]
	v_lshlrev_b32_e32 v8, 16, v9
	v_and_b32_e32 v9, 0xffff0000, v9
	v_add_f32_e32 v0, v22, v37
	v_pk_fma_f32 v[8:9], s[12:13], v[8:9], v[12:13] op_sel_hi:[0,1,1]
	v_lshlrev_b32_e32 v4, 16, v5
	v_and_b32_e32 v5, 0xffff0000, v5
	v_add_f32_e32 v14, v23, v0
	v_pk_fma_f32 v[4:5], s[18:19], v[4:5], v[8:9] op_sel_hi:[0,1,1]
	v_lshlrev_b32_e32 v0, 16, v1
	v_and_b32_e32 v1, 0xffff0000, v1
	v_pk_fma_f32 v[0:1], s[24:25], v[0:1], v[4:5] op_sel_hi:[0,1,1]
	v_add_f32_e32 v4, v0, v14
	v_lshlrev_b32_e32 v120, 16, v88
	v_and_b32_e32 v121, 0xffff0000, v88
	v_add_f32_e32 v12, v1, v4
	v_pk_fma_f32 v[4:5], s[22:23], v[94:95], v[90:91] op_sel_hi:[0,1,1]
	v_pk_fma_f32 v[4:5], s[20:21], v[120:121], v[4:5] op_sel_hi:[0,1,1]
	v_lshlrev_b32_e32 v124, 16, v96
	v_and_b32_e32 v125, 0xffff0000, v96
	v_pk_fma_f32 v[4:5], s[16:17], v[122:123], v[4:5] op_sel_hi:[0,1,1]
	v_pk_fma_f32 v[4:5], s[14:15], v[124:125], v[4:5] op_sel_hi:[0,1,1]
	v_lshlrev_b32_e32 v8, 16, v10
	v_and_b32_e32 v9, 0xffff0000, v10
	v_pk_fma_f32 v[4:5], s[12:13], v[8:9], v[4:5] op_sel_hi:[0,1,1]
	v_lshlrev_b32_e32 v8, 16, v6
	v_and_b32_e32 v9, 0xffff0000, v6
	v_pk_fma_f32 v[4:5], s[18:19], v[8:9], v[4:5] op_sel_hi:[0,1,1]
	v_lshlrev_b32_e32 v8, 16, v2
	v_and_b32_e32 v9, 0xffff0000, v2
	v_lshlrev_b32_e32 v80, 16, v89
	v_and_b32_e32 v81, 0xffff0000, v89
	v_pk_fma_f32 v[42:43], s[24:25], v[8:9], v[4:5] op_sel_hi:[0,1,1]
	v_pk_fma_f32 v[4:5], s[22:23], v[76:77], v[72:73] op_sel_hi:[0,1,1]
	v_pk_fma_f32 v[4:5], s[20:21], v[80:81], v[4:5] op_sel_hi:[0,1,1]
	v_lshlrev_b32_e32 v88, 16, v97
	v_and_b32_e32 v89, 0xffff0000, v97
	v_pk_fma_f32 v[4:5], s[16:17], v[84:85], v[4:5] op_sel_hi:[0,1,1]
	v_pk_fma_f32 v[4:5], s[14:15], v[88:89], v[4:5] op_sel_hi:[0,1,1]
	v_lshlrev_b32_e32 v8, 16, v11
	v_and_b32_e32 v9, 0xffff0000, v11
	v_add_f32_e32 v2, v42, v12
	v_pk_fma_f32 v[4:5], s[12:13], v[8:9], v[4:5] op_sel_hi:[0,1,1]
	v_lshlrev_b32_e32 v6, 16, v7
	v_and_b32_e32 v7, 0xffff0000, v7
	v_add_f32_e32 v10, v43, v2
	v_pk_fma_f32 v[4:5], s[18:19], v[6:7], v[4:5] op_sel_hi:[0,1,1]
	v_lshlrev_b32_e32 v2, 16, v3
	v_and_b32_e32 v3, 0xffff0000, v3
	v_pk_fma_f32 v[2:3], s[24:25], v[2:3], v[4:5] op_sel_hi:[0,1,1]
	v_add_f32_e32 v4, v2, v10
	v_add_f32_e32 v4, v3, v4
	s_nop 1
	v_add_f32_dpp v4, v4, v4 quad_perm:[1,0,3,2] row_mask:0xf bank_mask:0xf bound_ctrl:1
	s_nop 1
	v_add_f32_dpp v4, v4, v4 quad_perm:[2,3,0,1] row_mask:0xf bank_mask:0xf bound_ctrl:1
	s_nop 1
	v_add_f32_dpp v4, v4, v4 row_half_mirror row_mask:0xf bank_mask:0xf bound_ctrl:1
	s_nop 1
	v_add_f32_dpp v4, v4, v4 row_mirror row_mask:0xf bank_mask:0xf bound_ctrl:1
	v_mov_b32_e32 v5, v4
	s_nop 1
	v_permlane16_swap_b32 v5, v4
	s_nop 0
	v_add_f32_e32 v4, v5, v4
	v_mov_b32_e32 v5, v4
	s_nop 1
	v_permlane32_swap_b32 v4, v5
	s_nop 0
	v_add_f32_e32 v4, v4, v5
	v_mul_f32_e32 v44, 0x3a800000, v4
	v_pk_add_f32 v[12:13], v[46:47], v[44:45] op_sel_hi:[1,0] neg_lo:[0,1] neg_hi:[0,1]
	v_pk_add_f32 v[14:15], v[16:17], v[44:45] op_sel_hi:[1,0] neg_lo:[0,1] neg_hi:[0,1]
	v_pk_mul_f32 v[46:47], v[12:13], v[12:13]
	v_pk_mul_f32 v[16:17], v[14:15], v[14:15]
	v_add_f32_e32 v37, v46, v47
	v_pk_add_f32 v[8:9], v[20:21], v[44:45] op_sel_hi:[1,0] neg_lo:[0,1] neg_hi:[0,1]
	v_add_f32_e32 v16, v16, v37
	v_pk_mul_f32 v[20:21], v[8:9], v[8:9]
	v_add_f32_e32 v16, v17, v16
	v_pk_add_f32 v[10:11], v[18:19], v[44:45] op_sel_hi:[1,0] neg_lo:[0,1] neg_hi:[0,1]
	v_add_f32_e32 v16, v20, v16
	v_pk_mul_f32 v[18:19], v[10:11], v[10:11]
	v_add_f32_e32 v16, v21, v16
	v_pk_add_f32 v[4:5], v[22:23], v[44:45] op_sel_hi:[1,0] neg_lo:[0,1] neg_hi:[0,1]
	v_add_f32_e32 v16, v18, v16
	v_pk_mul_f32 v[22:23], v[4:5], v[4:5]
	v_add_f32_e32 v16, v19, v16
	v_pk_add_f32 v[6:7], v[0:1], v[44:45] op_sel_hi:[1,0] neg_lo:[0,1] neg_hi:[0,1]
	v_add_f32_e32 v16, v22, v16
	v_pk_mul_f32 v[48:49], v[6:7], v[6:7]
	v_add_f32_e32 v16, v23, v16
	v_pk_add_f32 v[0:1], v[42:43], v[44:45] op_sel_hi:[1,0] neg_lo:[0,1] neg_hi:[0,1]
	v_add_f32_e32 v16, v48, v16
	v_pk_mul_f32 v[42:43], v[0:1], v[0:1]
	v_add_f32_e32 v16, v49, v16
	v_pk_add_f32 v[2:3], v[2:3], v[44:45] op_sel_hi:[1,0] neg_lo:[0,1] neg_hi:[0,1]
	v_add_f32_e32 v16, v42, v16
	v_pk_mul_f32 v[44:45], v[2:3], v[2:3]
	v_add_f32_e32 v16, v43, v16
	v_add_f32_e32 v16, v44, v16
	v_add_f32_e32 v16, v45, v16
	s_nop 1
	v_add_f32_dpp v16, v16, v16 quad_perm:[1,0,3,2] row_mask:0xf bank_mask:0xf bound_ctrl:1
	s_nop 1
	v_add_f32_dpp v16, v16, v16 quad_perm:[2,3,0,1] row_mask:0xf bank_mask:0xf bound_ctrl:1
	s_nop 1
	v_add_f32_dpp v16, v16, v16 row_half_mirror row_mask:0xf bank_mask:0xf bound_ctrl:1
	s_nop 1
	v_add_f32_dpp v16, v16, v16 row_mirror row_mask:0xf bank_mask:0xf bound_ctrl:1
	v_mov_b32_e32 v17, v16
	s_nop 1
	v_permlane16_swap_b32 v17, v16
	s_nop 0
	v_add_f32_e32 v16, v17, v16
	v_mov_b32_e32 v17, v16
	s_nop 1
	v_permlane32_swap_b32 v17, v16
	s_cbranch_vccnz .LBB0_2590
	v_add_f32_e32 v16, v17, v16
	v_fmamk_f32 v16, v16, 0x3a800000, v25
	v_mul_f32_e32 v17, 0x4b800000, v16
	v_cmp_gt_f32_e32 vcc, s15, v16
	s_nop 1
	v_cndmask_b32_e32 v16, v16, v17, vcc
	v_rsq_f32_e32 v16, v16
	s_nop 0
	v_mul_f32_e32 v17, 0x45800000, v16
	v_cndmask_b32_e32 v22, v16, v17, vcc
	v_pk_mul_f32 v[12:13], v[12:13], v[22:23] op_sel_hi:[1,0]
	v_pk_mul_f32 v[14:15], v[14:15], v[22:23] op_sel_hi:[1,0]
	v_pk_mul_f32 v[8:9], v[8:9], v[22:23] op_sel_hi:[1,0]
	v_pk_mul_f32 v[10:11], v[10:11], v[22:23] op_sel_hi:[1,0]
	v_pk_mul_f32 v[4:5], v[4:5], v[22:23] op_sel_hi:[1,0]
	v_pk_mul_f32 v[6:7], v[6:7], v[22:23] op_sel_hi:[1,0]
	v_pk_mul_f32 v[0:1], v[0:1], v[22:23] op_sel_hi:[1,0]
	v_pk_mul_f32 v[2:3], v[2:3], v[22:23] op_sel_hi:[1,0]
	v_pk_fma_f32 v[12:13], v[12:13], v[200:201], v[204:205]
	v_pk_fma_f32 v[14:15], v[14:15], v[202:203], v[206:207]
	global_store_dwordx4 v[40:41], v[12:15], off offset:-2048
	v_pk_fma_f32 v[8:9], v[8:9], v[208:209], v[212:213]
	v_pk_fma_f32 v[10:11], v[10:11], v[210:211], v[214:215]
	global_store_dwordx4 v[40:41], v[8:11], off offset:-2032
	v_pk_fma_f32 v[4:5], v[4:5], v[216:217], v[220:221]
	v_pk_fma_f32 v[6:7], v[6:7], v[218:219], v[222:223]
	global_store_dwordx4 v[40:41], v[4:7], off
	v_pk_fma_f32 v[0:1], v[0:1], v[224:225], v[228:229]
	v_pk_fma_f32 v[2:3], v[2:3], v[226:227], v[230:231]
	global_store_dwordx4 v[40:41], v[0:3], off offset:16
	s_branch .LBB0_2590

	.amdhsa_kernel _Z7k_fused5KArgs
		.amdhsa_group_segment_fixed_size 0
		.amdhsa_private_segment_fixed_size 0
		.amdhsa_kernarg_size 472
		.amdhsa_user_sgpr_count 2
		.amdhsa_user_sgpr_dispatch_ptr 0
		.amdhsa_user_sgpr_queue_ptr 0
		.amdhsa_user_sgpr_kernarg_segment_ptr 1
		.amdhsa_user_sgpr_dispatch_id 0
		.amdhsa_user_sgpr_kernarg_preload_length 0
		.amdhsa_user_sgpr_kernarg_preload_offset 0
		.amdhsa_user_sgpr_private_segment_size 0
		.amdhsa_uses_dynamic_stack 0
		.amdhsa_enable_private_segment 0
		.amdhsa_system_sgpr_workgroup_id_x 1
		.amdhsa_system_sgpr_workgroup_id_y 0
		.amdhsa_system_sgpr_workgroup_id_z 0
		.amdhsa_system_sgpr_workgroup_info 0
		.amdhsa_system_vgpr_workitem_id 0
		.amdhsa_next_free_vgpr 256
		.amdhsa_next_free_sgpr 100
		.amdhsa_accum_offset 256
		.amdhsa_reserve_vcc 1
		.amdhsa_float_round_mode_32 0
		.amdhsa_float_round_mode_16_64 0
		.amdhsa_float_denorm_mode_32 3
		.amdhsa_float_denorm_mode_16_64 3
		.amdhsa_dx10_clamp 1
		.amdhsa_ieee_mode 1
		.amdhsa_fp16_overflow 0
		.amdhsa_tg_split 0
		.amdhsa_exception_fp_ieee_invalid_op 0
		.amdhsa_exception_fp_denorm_src 0
		.amdhsa_exception_fp_ieee_div_zero 0
		.amdhsa_exception_fp_ieee_overflow 0
		.amdhsa_exception_fp_ieee_underflow 0
		.amdhsa_exception_fp_ieee_inexact 0
		.amdhsa_exception_int_div_zero 0
	.end_amdhsa_kernel

amdhsa.kernels:
  - .agpr_count:     0
    .args:
      - .offset:         0
        .size:           216
        .value_kind:     by_value
      - .offset:         216
        .size:           4
        .value_kind:     hidden_block_count_x
      - .offset:         220
        .size:           4
        .value_kind:     hidden_block_count_y
      - .offset:         224
        .size:           4
        .value_kind:     hidden_block_count_z
      - .offset:         228
        .size:           2
        .value_kind:     hidden_group_size_x
      - .offset:         230
        .size:           2
        .value_kind:     hidden_group_size_y
      - .offset:         232
        .size:           2
        .value_kind:     hidden_group_size_z
      - .offset:         234
        .size:           2
        .value_kind:     hidden_remainder_x
      - .offset:         236
        .size:           2
        .value_kind:     hidden_remainder_y
      - .offset:         238
        .size:           2
        .value_kind:     hidden_remainder_z
      - .offset:         256
        .size:           8
        .value_kind:     hidden_global_offset_x
      - .offset:         264
        .size:           8
        .value_kind:     hidden_global_offset_y
      - .offset:         272
        .size:           8
        .value_kind:     hidden_global_offset_z
      - .offset:         280
        .size:           2
        .value_kind:     hidden_grid_dims
      - .offset:         336
        .size:           4
        .value_kind:     hidden_dynamic_lds_size
    .group_segment_fixed_size: 0
    .kernarg_segment_align: 8
    .kernarg_segment_size: 472
    .language:       OpenCL C
    .language_version:
      - 2
      - 0
    .max_flat_workgroup_size: 512
    .name:           _Z7k_fused5KArgs
    .private_segment_fixed_size: 0
    .sgpr_count:     106
    .sgpr_spill_count: 150
    .symbol:         _Z7k_fused5KArgs.kd
    .uniform_work_group_size: 1
    .uses_dynamic_stack: false
    .vgpr_count:     256
    .vgpr_spill_count: 0
    .wavefront_size: 64
